# baseline (speedup 1.0000x reference)
.Lp_main:
	s_load_dwordx2 s[10:11], s[0:1], 0x0
	s_load_dwordx4 s[12:15], s[0:1], 0x10
	s_load_dwordx2 s[16:17], s[0:1], 0x20
	s_load_dwordx4 s[20:23], s[0:1], 0x28
	v_readfirstlane_b32 s3, v0
	v_and_b32_e32 v154, 63, v0
	v_lshrrev_b32_e32 v155, 5, v154
	v_lshlrev_b32_e32 v156, 4, v0
	v_lshlrev_b32_e32 v157, 4, v154
	v_lshlrev_b32_e32 v158, 8, v1
	v_lshl_add_u32 v158, v155, 5, v158
	v_lshlrev_b32_e32 v159, 4, v155
	v_lshrrev_b32_e32 v160, 3, v0
	v_lshlrev_b32_e32 v160, 12, v160
	v_and_b32_e32 v161, 7, v0
	v_lshl_add_u32 v160, v161, 4, v160
	s_lshr_b32 s41, s2, 3
	s_and_b32 s42, s2, 7
	s_lshl_b32 s24, s42, 2
	s_bfe_u32 s25, s2, 0x20003
	s_add_u32 s24, s24, s25
	s_lshr_b32 s25, s2, 5
	s_lshr_b32 s26, s3, 6
	s_lshl_b32 s27, s25, 2
	s_add_u32 s27, s27, s26
	s_mov_b32 s4, 0x4038aa3b
	s_mov_b32 s5, s4
	s_lshl_b32 s40, s26, 6
	s_waitcnt lgkmcnt(0)
	s_lshl_b32 s28, s24, 15
	s_add_u32 s28, s28, 0x1000
	s_add_u32 s10, s10, s28
	s_addc_u32 s11, s11, 0
	s_lshl_b32 s34, s41, 17
	s_lshl_b32 s35, s42, 9
	s_add_u32 s34, s34, s35
	s_add_u32 s34, s14, s34
	s_addc_u32 s35, s15, 0
	s_lshl_b32 s28, s27, 13
	s_add_u32 s28, s8, s28
	s_addc_u32 s29, s9, 0
	s_lshl_b32 s30, s27, 7
	s_add_u32 s30, s12, s30
	s_addc_u32 s31, s13, 0
	global_load_dwordx4 v[2:5], v156, s[10:11] offset:-4096
	global_load_dwordx4 v[6:9], v156, s[10:11] offset:0
	s_add_u32 s10, s10, 0x2000
	s_addc_u32 s11, s11, 0
	global_load_dwordx4 v[10:13], v156, s[10:11] offset:-4096
	global_load_dwordx4 v[14:17], v156, s[10:11] offset:0
	s_add_u32 s10, s10, 0x2000
	s_addc_u32 s11, s11, 0
	global_load_dwordx4 v[18:21], v156, s[10:11] offset:-4096
	global_load_dwordx4 v[22:25], v156, s[10:11] offset:0
	s_add_u32 s10, s10, 0x2000
	s_addc_u32 s11, s11, 0
	global_load_dwordx4 v[26:29], v156, s[10:11] offset:-4096
	global_load_dwordx4 v[30:33], v156, s[10:11] offset:0
	global_load_dwordx4 v[34:37], v158, s[28:29] offset:0
	global_load_dwordx4 v[38:41], v158, s[28:29] offset:16
	global_load_dwordx4 v[42:45], v158, s[28:29] offset:64
	global_load_dwordx4 v[46:49], v158, s[28:29] offset:80
	global_load_dwordx4 v[50:53], v158, s[28:29] offset:128
	global_load_dwordx4 v[54:57], v158, s[28:29] offset:144
	global_load_dwordx4 v[58:61], v158, s[28:29] offset:192
	global_load_dwordx4 v[62:65], v158, s[28:29] offset:208
	global_load_dwordx4 v[66:69], v159, s[30:31] offset:0
	global_load_dwordx4 v[70:73], v159, s[30:31] offset:32
	global_load_dwordx4 v[74:77], v159, s[30:31] offset:64
	global_load_dwordx4 v[78:81], v159, s[30:31] offset:96
	v_bfe_u32 v163, v0, 1, 3
	v_mul_u32_u24_e32 v163, 0x210, v163
	v_lshrrev_b32_e32 v164, 4, v0
	v_lshl_add_u32 v163, v164, 4, v163
	v_and_b32_e32 v164, 1, v0
	v_lshl_add_u32 v163, v164, 3, v163
	v_lshrrev_b32_e32 v164, 3, v0
	v_mul_u32_u24_e32 v164, 0x110, v164
	v_lshl_add_u32 v164, v161, 3, v164
	v_add_u32_e32 v164, 0x4200, v164
	v_mul_u32_u24_e32 v165, 0x210, v155
	v_lshl_add_u32 v165, v1, 4, v165
	v_mul_u32_u24_e32 v166, 0x110, v1
	v_lshl_add_u32 v166, v155, 4, v166
	v_add_u32_e32 v166, s40, v166
	v_add_u32_e32 v166, 0x4200, v166
	v_mul_u32_u24_e32 v167, 0x880, v155
	v_lshl_add_u32 v167, v1, 1, v167
	v_add_u32_e32 v167, s40, v167
	v_add_u32_e32 v167, 0x4200, v167
	s_lshl_b32 s32, s24, 18
	s_lshl_b32 s33, s27, 11
	s_add_u32 s32, s32, s33
	s_add_u32 s32, s16, s32
	s_addc_u32 s33, s17, 0
	s_lshl_b32 s36, s41, 16
	s_lshl_b32 s37, s42, 13
	s_add_u32 s36, s36, s37
	s_lshl_b32 s37, s26, 11
	s_add_u32 s36, s36, s37
	s_add_u32 s36, s20, s36
	s_addc_u32 s37, s21, 0
	s_lshl_b32 s38, s42, 18
	s_lshl_b32 s39, s26, 16
	s_add_u32 s38, s38, s39
	s_lshl_b32 s39, s41, 11
	s_add_u32 s38, s38, s39
	s_add_u32 s38, s22, s38
	s_addc_u32 s39, s23, 0
	s_waitcnt vmcnt(19)
	v_cvt_pk_f16_f32 v2, v2, v3
	v_cvt_pk_f16_f32 v3, v4, v5
	ds_write_b64 v163, v[2:3] offset:0
	s_waitcnt vmcnt(18)
	v_cvt_pk_f16_f32 v6, v6, v7
	v_cvt_pk_f16_f32 v7, v8, v9
	ds_write_b64 v163, v[6:7] offset:256
	s_waitcnt vmcnt(17)
	v_cvt_pk_f16_f32 v10, v10, v11
	v_cvt_pk_f16_f32 v11, v12, v13
	ds_write_b64 v163, v[10:11] offset:4224
	s_waitcnt vmcnt(16)
	v_cvt_pk_f16_f32 v14, v14, v15
	v_cvt_pk_f16_f32 v15, v16, v17
	ds_write_b64 v163, v[14:15] offset:4480
	s_waitcnt vmcnt(15)
	v_cvt_pk_f16_f32 v18, v18, v19
	v_cvt_pk_f16_f32 v19, v20, v21
	ds_write_b64 v163, v[18:19] offset:8448
	s_waitcnt vmcnt(14)
	v_cvt_pk_f16_f32 v22, v22, v23
	v_cvt_pk_f16_f32 v23, v24, v25
	ds_write_b64 v163, v[22:23] offset:8704
	s_waitcnt vmcnt(13)
	v_cvt_pk_f16_f32 v26, v26, v27
	v_cvt_pk_f16_f32 v27, v28, v29
	ds_write_b64 v163, v[26:27] offset:12672
	s_waitcnt vmcnt(12)
	v_cvt_pk_f16_f32 v30, v30, v31
	v_cvt_pk_f16_f32 v31, v32, v33
	ds_write_b64 v163, v[30:31] offset:12928
	global_load_dwordx4 v[168:171], v160, s[34:35] offset:0
	global_load_dwordx4 v[172:175], v160, s[34:35] offset:128
	global_load_dwordx4 v[176:179], v160, s[34:35] offset:256
	global_load_dwordx4 v[180:183], v160, s[34:35] offset:384
	s_waitcnt lgkmcnt(0)
	s_barrier
	ds_read_b128 v[2:5], v165 offset:0
	ds_read_b128 v[6:9], v165 offset:1056
	ds_read_b128 v[10:13], v165 offset:2112
	ds_read_b128 v[14:17], v165 offset:3168
	ds_read_b128 v[18:21], v165 offset:4224
	ds_read_b128 v[22:25], v165 offset:5280
	ds_read_b128 v[26:29], v165 offset:6336
	ds_read_b128 v[30:33], v165 offset:7392
	s_waitcnt vmcnt(8)
	v_cvt_pk_f16_f32 v82, v34, v35
	v_cvt_pk_f16_f32 v83, v36, v37
	v_cvt_pk_f16_f32 v84, v38, v39
	v_cvt_pk_f16_f32 v85, v40, v41
	v_cvt_pk_f16_f32 v86, v42, v43
	v_cvt_pk_f16_f32 v87, v44, v45
	v_cvt_pk_f16_f32 v88, v46, v47
	v_cvt_pk_f16_f32 v89, v48, v49
	v_cvt_pk_f16_f32 v90, v50, v51
	v_cvt_pk_f16_f32 v91, v52, v53
	v_cvt_pk_f16_f32 v92, v54, v55
	v_cvt_pk_f16_f32 v93, v56, v57
	v_cvt_pk_f16_f32 v94, v58, v59
	v_cvt_pk_f16_f32 v95, v60, v61
	v_cvt_pk_f16_f32 v96, v62, v63
	v_cvt_pk_f16_f32 v97, v64, v65
	ds_read_b128 v[34:37], v165 offset:8448
	ds_read_b128 v[38:41], v165 offset:9504
	ds_read_b128 v[42:45], v165 offset:10560
	ds_read_b128 v[46:49], v165 offset:11616
	s_waitcnt vmcnt(4)
	v_pk_mul_f32 v[66:67], v[66:67], s[4:5] op_sel_hi:[1,0]
	v_pk_mul_f32 v[68:69], v[68:69], s[4:5] op_sel_hi:[1,0]
	v_pk_mul_f32 v[70:71], v[70:71], s[4:5] op_sel_hi:[1,0]
	v_pk_mul_f32 v[72:73], v[72:73], s[4:5] op_sel_hi:[1,0]
	v_pk_mul_f32 v[74:75], v[74:75], s[4:5] op_sel_hi:[1,0]
	v_pk_mul_f32 v[76:77], v[76:77], s[4:5] op_sel_hi:[1,0]
	v_pk_mul_f32 v[78:79], v[78:79], s[4:5] op_sel_hi:[1,0]
	v_pk_mul_f32 v[80:81], v[80:81], s[4:5] op_sel_hi:[1,0]
	s_waitcnt lgkmcnt(8)
	v_mfma_f32_32x32x16_f16 v[98:113], v[82:85], v[2:5], 0
	v_mfma_f32_32x32x16_f16 v[98:113], v[86:89], v[6:9], v[98:113]
	v_mfma_f32_32x32x16_f16 v[98:113], v[90:93], v[10:13], v[98:113]
	v_mfma_f32_32x32x16_f16 v[98:113], v[94:97], v[14:17], v[98:113]
	ds_read_b128 v[50:53], v165 offset:12672
	ds_read_b128 v[54:57], v165 offset:13728
	ds_read_b128 v[58:61], v165 offset:14784
	ds_read_b128 v[62:65], v165 offset:15840
	s_waitcnt lgkmcnt(8)
	v_mfma_f32_32x32x16_f16 v[114:129], v[82:85], v[18:21], 0
	v_mfma_f32_32x32x16_f16 v[114:129], v[86:89], v[22:25], v[114:129]
	v_mfma_f32_32x32x16_f16 v[114:129], v[90:93], v[26:29], v[114:129]
	v_mfma_f32_32x32x16_f16 v[114:129], v[94:97], v[30:33], v[114:129]
	s_nop 7
	v_pk_fma_f32 v[130:131], v[98:99], s[4:5], v[66:67] op_sel_hi:[1,0,1]
	v_pk_fma_f32 v[132:133], v[100:101], s[4:5], v[68:69] op_sel_hi:[1,0,1]
	v_pk_fma_f32 v[134:135], v[102:103], s[4:5], v[70:71] op_sel_hi:[1,0,1]
	v_pk_fma_f32 v[136:137], v[104:105], s[4:5], v[72:73] op_sel_hi:[1,0,1]
	v_pk_fma_f32 v[138:139], v[106:107], s[4:5], v[74:75] op_sel_hi:[1,0,1]
	v_pk_fma_f32 v[140:141], v[108:109], s[4:5], v[76:77] op_sel_hi:[1,0,1]
	v_pk_fma_f32 v[142:143], v[110:111], s[4:5], v[78:79] op_sel_hi:[1,0,1]
	v_pk_fma_f32 v[144:145], v[112:113], s[4:5], v[80:81] op_sel_hi:[1,0,1]
	v_exp_f32_e32 v130, v130
	v_exp_f32_e32 v131, v131
	v_exp_f32_e32 v132, v132
	v_exp_f32_e32 v133, v133
	v_exp_f32_e32 v134, v134
	v_exp_f32_e32 v135, v135
	v_exp_f32_e32 v136, v136
	v_exp_f32_e32 v137, v137
	v_exp_f32_e32 v138, v138
	v_exp_f32_e32 v139, v139
	v_exp_f32_e32 v140, v140
	v_exp_f32_e32 v141, v141
	v_exp_f32_e32 v142, v142
	v_exp_f32_e32 v143, v143
	v_exp_f32_e32 v144, v144
	v_exp_f32_e32 v145, v145
	v_pk_add_f32 v[130:131], v[130:131], 1.0 op_sel_hi:[1,0]
	v_pk_add_f32 v[132:133], v[132:133], 1.0 op_sel_hi:[1,0]
	v_pk_add_f32 v[134:135], v[134:135], 1.0 op_sel_hi:[1,0]
	v_pk_add_f32 v[136:137], v[136:137], 1.0 op_sel_hi:[1,0]
	v_pk_add_f32 v[138:139], v[138:139], 1.0 op_sel_hi:[1,0]
	v_pk_add_f32 v[140:141], v[140:141], 1.0 op_sel_hi:[1,0]
	v_pk_add_f32 v[142:143], v[142:143], 1.0 op_sel_hi:[1,0]
	v_pk_add_f32 v[144:145], v[144:145], 1.0 op_sel_hi:[1,0]
	v_rcp_f32_e32 v130, v130
	v_rcp_f32_e32 v131, v131
	v_rcp_f32_e32 v132, v132
	v_rcp_f32_e32 v133, v133
	v_rcp_f32_e32 v134, v134
	v_rcp_f32_e32 v135, v135
	v_rcp_f32_e32 v136, v136
	v_rcp_f32_e32 v137, v137
	v_rcp_f32_e32 v138, v138
	v_rcp_f32_e32 v139, v139
	v_rcp_f32_e32 v140, v140
	v_rcp_f32_e32 v141, v141
	v_rcp_f32_e32 v142, v142
	v_rcp_f32_e32 v143, v143
	v_rcp_f32_e32 v144, v144
	v_rcp_f32_e32 v145, v145
	v_pk_fma_f32 v[130:131], v[130:131], 2.0, 1.0 op_sel_hi:[1,0,0] neg_lo:[1,0,0] neg_hi:[1,0,0]
	v_pk_fma_f32 v[132:133], v[132:133], 2.0, 1.0 op_sel_hi:[1,0,0] neg_lo:[1,0,0] neg_hi:[1,0,0]
	v_pk_fma_f32 v[134:135], v[134:135], 2.0, 1.0 op_sel_hi:[1,0,0] neg_lo:[1,0,0] neg_hi:[1,0,0]
	v_pk_fma_f32 v[136:137], v[136:137], 2.0, 1.0 op_sel_hi:[1,0,0] neg_lo:[1,0,0] neg_hi:[1,0,0]
	v_pk_fma_f32 v[138:139], v[138:139], 2.0, 1.0 op_sel_hi:[1,0,0] neg_lo:[1,0,0] neg_hi:[1,0,0]
	v_pk_fma_f32 v[140:141], v[140:141], 2.0, 1.0 op_sel_hi:[1,0,0] neg_lo:[1,0,0] neg_hi:[1,0,0]
	v_pk_fma_f32 v[142:143], v[142:143], 2.0, 1.0 op_sel_hi:[1,0,0] neg_lo:[1,0,0] neg_hi:[1,0,0]
	v_pk_fma_f32 v[144:145], v[144:145], 2.0, 1.0 op_sel_hi:[1,0,0] neg_lo:[1,0,0] neg_hi:[1,0,0]
	v_cvt_pk_f16_f32 v146, v130, v131
	v_cvt_pk_f16_f32 v147, v132, v133
	v_cvt_pk_f16_f32 v148, v134, v135
	v_cvt_pk_f16_f32 v149, v136, v137
	v_cvt_pk_f16_f32 v150, v138, v139
	v_cvt_pk_f16_f32 v151, v140, v141
	v_cvt_pk_f16_f32 v152, v142, v143
	v_cvt_pk_f16_f32 v153, v144, v145
	s_nop 1
	v_permlane32_swap_b32_e32 v146, v148
	v_permlane32_swap_b32_e32 v147, v149
	v_permlane32_swap_b32_e32 v150, v152
	v_permlane32_swap_b32_e32 v151, v153
	global_store_dwordx4 v157, v[146:149], s[32:33] sc1
	global_store_dwordx4 v157, v[150:153], s[32:33] offset:1024 sc1
	s_add_u32 s32, s32, 0x10000
	s_addc_u32 s33, s33, 0
	s_waitcnt lgkmcnt(4)
	v_mfma_f32_32x32x16_f16 v[98:113], v[82:85], v[34:37], 0
	v_mfma_f32_32x32x16_f16 v[98:113], v[86:89], v[38:41], v[98:113]
	v_mfma_f32_32x32x16_f16 v[98:113], v[90:93], v[42:45], v[98:113]
	v_mfma_f32_32x32x16_f16 v[98:113], v[94:97], v[46:49], v[98:113]
	v_pk_fma_f32 v[130:131], v[114:115], s[4:5], v[66:67] op_sel_hi:[1,0,1]
	v_pk_fma_f32 v[132:133], v[116:117], s[4:5], v[68:69] op_sel_hi:[1,0,1]
	v_pk_fma_f32 v[134:135], v[118:119], s[4:5], v[70:71] op_sel_hi:[1,0,1]
	v_pk_fma_f32 v[136:137], v[120:121], s[4:5], v[72:73] op_sel_hi:[1,0,1]
	v_pk_fma_f32 v[138:139], v[122:123], s[4:5], v[74:75] op_sel_hi:[1,0,1]
	v_pk_fma_f32 v[140:141], v[124:125], s[4:5], v[76:77] op_sel_hi:[1,0,1]
	v_pk_fma_f32 v[142:143], v[126:127], s[4:5], v[78:79] op_sel_hi:[1,0,1]
	v_pk_fma_f32 v[144:145], v[128:129], s[4:5], v[80:81] op_sel_hi:[1,0,1]
	v_exp_f32_e32 v130, v130
	v_exp_f32_e32 v131, v131
	v_exp_f32_e32 v132, v132
	v_exp_f32_e32 v133, v133
	v_exp_f32_e32 v134, v134
	v_exp_f32_e32 v135, v135
	v_exp_f32_e32 v136, v136
	v_exp_f32_e32 v137, v137
	v_exp_f32_e32 v138, v138
	v_exp_f32_e32 v139, v139
	v_exp_f32_e32 v140, v140
	v_exp_f32_e32 v141, v141
	v_exp_f32_e32 v142, v142
	v_exp_f32_e32 v143, v143
	v_exp_f32_e32 v144, v144
	v_exp_f32_e32 v145, v145
	v_pk_add_f32 v[130:131], v[130:131], 1.0 op_sel_hi:[1,0]
	v_pk_add_f32 v[132:133], v[132:133], 1.0 op_sel_hi:[1,0]
	v_pk_add_f32 v[134:135], v[134:135], 1.0 op_sel_hi:[1,0]
	v_pk_add_f32 v[136:137], v[136:137], 1.0 op_sel_hi:[1,0]
	v_pk_add_f32 v[138:139], v[138:139], 1.0 op_sel_hi:[1,0]
	v_pk_add_f32 v[140:141], v[140:141], 1.0 op_sel_hi:[1,0]
	v_pk_add_f32 v[142:143], v[142:143], 1.0 op_sel_hi:[1,0]
	v_pk_add_f32 v[144:145], v[144:145], 1.0 op_sel_hi:[1,0]
	v_rcp_f32_e32 v130, v130
	v_rcp_f32_e32 v131, v131
	v_rcp_f32_e32 v132, v132
	v_rcp_f32_e32 v133, v133
	v_rcp_f32_e32 v134, v134
	v_rcp_f32_e32 v135, v135
	v_rcp_f32_e32 v136, v136
	v_rcp_f32_e32 v137, v137
	v_rcp_f32_e32 v138, v138
	v_rcp_f32_e32 v139, v139
	v_rcp_f32_e32 v140, v140
	v_rcp_f32_e32 v141, v141
	v_rcp_f32_e32 v142, v142
	v_rcp_f32_e32 v143, v143
	v_rcp_f32_e32 v144, v144
	v_rcp_f32_e32 v145, v145
	v_pk_fma_f32 v[130:131], v[130:131], 2.0, 1.0 op_sel_hi:[1,0,0] neg_lo:[1,0,0] neg_hi:[1,0,0]
	v_pk_fma_f32 v[132:133], v[132:133], 2.0, 1.0 op_sel_hi:[1,0,0] neg_lo:[1,0,0] neg_hi:[1,0,0]
	v_pk_fma_f32 v[134:135], v[134:135], 2.0, 1.0 op_sel_hi:[1,0,0] neg_lo:[1,0,0] neg_hi:[1,0,0]
	v_pk_fma_f32 v[136:137], v[136:137], 2.0, 1.0 op_sel_hi:[1,0,0] neg_lo:[1,0,0] neg_hi:[1,0,0]
	v_pk_fma_f32 v[138:139], v[138:139], 2.0, 1.0 op_sel_hi:[1,0,0] neg_lo:[1,0,0] neg_hi:[1,0,0]
	v_pk_fma_f32 v[140:141], v[140:141], 2.0, 1.0 op_sel_hi:[1,0,0] neg_lo:[1,0,0] neg_hi:[1,0,0]
	v_pk_fma_f32 v[142:143], v[142:143], 2.0, 1.0 op_sel_hi:[1,0,0] neg_lo:[1,0,0] neg_hi:[1,0,0]
	v_pk_fma_f32 v[144:145], v[144:145], 2.0, 1.0 op_sel_hi:[1,0,0] neg_lo:[1,0,0] neg_hi:[1,0,0]
	v_cvt_pk_f16_f32 v146, v130, v131
	v_cvt_pk_f16_f32 v147, v132, v133
	v_cvt_pk_f16_f32 v148, v134, v135
	v_cvt_pk_f16_f32 v149, v136, v137
	v_cvt_pk_f16_f32 v150, v138, v139
	v_cvt_pk_f16_f32 v151, v140, v141
	v_cvt_pk_f16_f32 v152, v142, v143
	v_cvt_pk_f16_f32 v153, v144, v145
	s_nop 1
	v_permlane32_swap_b32_e32 v146, v148
	v_permlane32_swap_b32_e32 v147, v149
	v_permlane32_swap_b32_e32 v150, v152
	v_permlane32_swap_b32_e32 v151, v153
	global_store_dwordx4 v157, v[146:149], s[32:33] sc1
	global_store_dwordx4 v157, v[150:153], s[32:33] offset:1024 sc1
	s_add_u32 s32, s32, 0x10000
	s_addc_u32 s33, s33, 0
	s_waitcnt lgkmcnt(0)
	v_mfma_f32_32x32x16_f16 v[114:129], v[82:85], v[50:53], 0
	v_mfma_f32_32x32x16_f16 v[114:129], v[86:89], v[54:57], v[114:129]
	v_mfma_f32_32x32x16_f16 v[114:129], v[90:93], v[58:61], v[114:129]
	v_mfma_f32_32x32x16_f16 v[114:129], v[94:97], v[62:65], v[114:129]
	v_pk_fma_f32 v[130:131], v[98:99], s[4:5], v[66:67] op_sel_hi:[1,0,1]
	v_pk_fma_f32 v[132:133], v[100:101], s[4:5], v[68:69] op_sel_hi:[1,0,1]
	v_pk_fma_f32 v[134:135], v[102:103], s[4:5], v[70:71] op_sel_hi:[1,0,1]
	v_pk_fma_f32 v[136:137], v[104:105], s[4:5], v[72:73] op_sel_hi:[1,0,1]
	v_pk_fma_f32 v[138:139], v[106:107], s[4:5], v[74:75] op_sel_hi:[1,0,1]
	v_pk_fma_f32 v[140:141], v[108:109], s[4:5], v[76:77] op_sel_hi:[1,0,1]
	v_pk_fma_f32 v[142:143], v[110:111], s[4:5], v[78:79] op_sel_hi:[1,0,1]
	v_pk_fma_f32 v[144:145], v[112:113], s[4:5], v[80:81] op_sel_hi:[1,0,1]
	v_exp_f32_e32 v130, v130
	v_exp_f32_e32 v131, v131
	v_exp_f32_e32 v132, v132
	v_exp_f32_e32 v133, v133
	v_exp_f32_e32 v134, v134
	v_exp_f32_e32 v135, v135
	v_exp_f32_e32 v136, v136
	v_exp_f32_e32 v137, v137
	v_exp_f32_e32 v138, v138
	v_exp_f32_e32 v139, v139
	v_exp_f32_e32 v140, v140
	v_exp_f32_e32 v141, v141
	v_exp_f32_e32 v142, v142
	v_exp_f32_e32 v143, v143
	v_exp_f32_e32 v144, v144
	v_exp_f32_e32 v145, v145
	v_pk_add_f32 v[130:131], v[130:131], 1.0 op_sel_hi:[1,0]
	v_pk_add_f32 v[132:133], v[132:133], 1.0 op_sel_hi:[1,0]
	v_pk_add_f32 v[134:135], v[134:135], 1.0 op_sel_hi:[1,0]
	v_pk_add_f32 v[136:137], v[136:137], 1.0 op_sel_hi:[1,0]
	v_pk_add_f32 v[138:139], v[138:139], 1.0 op_sel_hi:[1,0]
	v_pk_add_f32 v[140:141], v[140:141], 1.0 op_sel_hi:[1,0]
	v_pk_add_f32 v[142:143], v[142:143], 1.0 op_sel_hi:[1,0]
	v_pk_add_f32 v[144:145], v[144:145], 1.0 op_sel_hi:[1,0]
	v_rcp_f32_e32 v130, v130
	v_rcp_f32_e32 v131, v131
	v_rcp_f32_e32 v132, v132
	v_rcp_f32_e32 v133, v133
	v_rcp_f32_e32 v134, v134
	v_rcp_f32_e32 v135, v135
	v_rcp_f32_e32 v136, v136
	v_rcp_f32_e32 v137, v137
	v_rcp_f32_e32 v138, v138
	v_rcp_f32_e32 v139, v139
	v_rcp_f32_e32 v140, v140
	v_rcp_f32_e32 v141, v141
	v_rcp_f32_e32 v142, v142
	v_rcp_f32_e32 v143, v143
	v_rcp_f32_e32 v144, v144
	v_rcp_f32_e32 v145, v145
	v_pk_fma_f32 v[130:131], v[130:131], 2.0, 1.0 op_sel_hi:[1,0,0] neg_lo:[1,0,0] neg_hi:[1,0,0]
	v_pk_fma_f32 v[132:133], v[132:133], 2.0, 1.0 op_sel_hi:[1,0,0] neg_lo:[1,0,0] neg_hi:[1,0,0]
	v_pk_fma_f32 v[134:135], v[134:135], 2.0, 1.0 op_sel_hi:[1,0,0] neg_lo:[1,0,0] neg_hi:[1,0,0]
	v_pk_fma_f32 v[136:137], v[136:137], 2.0, 1.0 op_sel_hi:[1,0,0] neg_lo:[1,0,0] neg_hi:[1,0,0]
	v_pk_fma_f32 v[138:139], v[138:139], 2.0, 1.0 op_sel_hi:[1,0,0] neg_lo:[1,0,0] neg_hi:[1,0,0]
	v_pk_fma_f32 v[140:141], v[140:141], 2.0, 1.0 op_sel_hi:[1,0,0] neg_lo:[1,0,0] neg_hi:[1,0,0]
	v_pk_fma_f32 v[142:143], v[142:143], 2.0, 1.0 op_sel_hi:[1,0,0] neg_lo:[1,0,0] neg_hi:[1,0,0]
	v_pk_fma_f32 v[144:145], v[144:145], 2.0, 1.0 op_sel_hi:[1,0,0] neg_lo:[1,0,0] neg_hi:[1,0,0]
	v_cvt_pk_f16_f32 v146, v130, v131
	v_cvt_pk_f16_f32 v147, v132, v133
	v_cvt_pk_f16_f32 v148, v134, v135
	v_cvt_pk_f16_f32 v149, v136, v137
	v_cvt_pk_f16_f32 v150, v138, v139
	v_cvt_pk_f16_f32 v151, v140, v141
	v_cvt_pk_f16_f32 v152, v142, v143
	v_cvt_pk_f16_f32 v153, v144, v145
	s_nop 1
	v_permlane32_swap_b32_e32 v146, v148
	v_permlane32_swap_b32_e32 v147, v149
	v_permlane32_swap_b32_e32 v150, v152
	v_permlane32_swap_b32_e32 v151, v153
	global_store_dwordx4 v157, v[146:149], s[32:33] sc1
	global_store_dwordx4 v157, v[150:153], s[32:33] offset:1024 sc1
	s_add_u32 s32, s32, 0x10000
	s_addc_u32 s33, s33, 0
	v_pk_fma_f32 v[130:131], v[114:115], s[4:5], v[66:67] op_sel_hi:[1,0,1]
	v_pk_fma_f32 v[132:133], v[116:117], s[4:5], v[68:69] op_sel_hi:[1,0,1]
	v_pk_fma_f32 v[134:135], v[118:119], s[4:5], v[70:71] op_sel_hi:[1,0,1]
	v_pk_fma_f32 v[136:137], v[120:121], s[4:5], v[72:73] op_sel_hi:[1,0,1]
	v_pk_fma_f32 v[138:139], v[122:123], s[4:5], v[74:75] op_sel_hi:[1,0,1]
	v_pk_fma_f32 v[140:141], v[124:125], s[4:5], v[76:77] op_sel_hi:[1,0,1]
	v_pk_fma_f32 v[142:143], v[126:127], s[4:5], v[78:79] op_sel_hi:[1,0,1]
	v_pk_fma_f32 v[144:145], v[128:129], s[4:5], v[80:81] op_sel_hi:[1,0,1]
	v_exp_f32_e32 v130, v130
	v_exp_f32_e32 v131, v131
	v_exp_f32_e32 v132, v132
	v_exp_f32_e32 v133, v133
	v_exp_f32_e32 v134, v134
	v_exp_f32_e32 v135, v135
	v_exp_f32_e32 v136, v136
	v_exp_f32_e32 v137, v137
	v_exp_f32_e32 v138, v138
	v_exp_f32_e32 v139, v139
	v_exp_f32_e32 v140, v140
	v_exp_f32_e32 v141, v141
	v_exp_f32_e32 v142, v142
	v_exp_f32_e32 v143, v143
	v_exp_f32_e32 v144, v144
	v_exp_f32_e32 v145, v145
	v_pk_add_f32 v[130:131], v[130:131], 1.0 op_sel_hi:[1,0]
	v_pk_add_f32 v[132:133], v[132:133], 1.0 op_sel_hi:[1,0]
	v_pk_add_f32 v[134:135], v[134:135], 1.0 op_sel_hi:[1,0]
	v_pk_add_f32 v[136:137], v[136:137], 1.0 op_sel_hi:[1,0]
	v_pk_add_f32 v[138:139], v[138:139], 1.0 op_sel_hi:[1,0]
	v_pk_add_f32 v[140:141], v[140:141], 1.0 op_sel_hi:[1,0]
	v_pk_add_f32 v[142:143], v[142:143], 1.0 op_sel_hi:[1,0]
	v_pk_add_f32 v[144:145], v[144:145], 1.0 op_sel_hi:[1,0]
	v_rcp_f32_e32 v130, v130
	v_rcp_f32_e32 v131, v131
	v_rcp_f32_e32 v132, v132
	v_rcp_f32_e32 v133, v133
	v_rcp_f32_e32 v134, v134
	v_rcp_f32_e32 v135, v135
	v_rcp_f32_e32 v136, v136
	v_rcp_f32_e32 v137, v137
	v_rcp_f32_e32 v138, v138
	v_rcp_f32_e32 v139, v139
	v_rcp_f32_e32 v140, v140
	v_rcp_f32_e32 v141, v141
	v_rcp_f32_e32 v142, v142
	v_rcp_f32_e32 v143, v143
	v_rcp_f32_e32 v144, v144
	v_rcp_f32_e32 v145, v145
	v_pk_fma_f32 v[130:131], v[130:131], 2.0, 1.0 op_sel_hi:[1,0,0] neg_lo:[1,0,0] neg_hi:[1,0,0]
	v_pk_fma_f32 v[132:133], v[132:133], 2.0, 1.0 op_sel_hi:[1,0,0] neg_lo:[1,0,0] neg_hi:[1,0,0]
	v_pk_fma_f32 v[134:135], v[134:135], 2.0, 1.0 op_sel_hi:[1,0,0] neg_lo:[1,0,0] neg_hi:[1,0,0]
	v_pk_fma_f32 v[136:137], v[136:137], 2.0, 1.0 op_sel_hi:[1,0,0] neg_lo:[1,0,0] neg_hi:[1,0,0]
	v_pk_fma_f32 v[138:139], v[138:139], 2.0, 1.0 op_sel_hi:[1,0,0] neg_lo:[1,0,0] neg_hi:[1,0,0]
	v_pk_fma_f32 v[140:141], v[140:141], 2.0, 1.0 op_sel_hi:[1,0,0] neg_lo:[1,0,0] neg_hi:[1,0,0]
	v_pk_fma_f32 v[142:143], v[142:143], 2.0, 1.0 op_sel_hi:[1,0,0] neg_lo:[1,0,0] neg_hi:[1,0,0]
	v_pk_fma_f32 v[144:145], v[144:145], 2.0, 1.0 op_sel_hi:[1,0,0] neg_lo:[1,0,0] neg_hi:[1,0,0]
	v_cvt_pk_f16_f32 v146, v130, v131
	v_cvt_pk_f16_f32 v147, v132, v133
	v_cvt_pk_f16_f32 v148, v134, v135
	v_cvt_pk_f16_f32 v149, v136, v137
	v_cvt_pk_f16_f32 v150, v138, v139
	v_cvt_pk_f16_f32 v151, v140, v141
	v_cvt_pk_f16_f32 v152, v142, v143
	v_cvt_pk_f16_f32 v153, v144, v145
	s_nop 1
	v_permlane32_swap_b32_e32 v146, v148
	v_permlane32_swap_b32_e32 v147, v149
	v_permlane32_swap_b32_e32 v150, v152
	v_permlane32_swap_b32_e32 v151, v153
	global_store_dwordx4 v157, v[146:149], s[32:33] sc1
	global_store_dwordx4 v157, v[150:153], s[32:33] offset:1024 sc1
	s_waitcnt vmcnt(11)
	v_cvt_pk_f16_f32 v168, v168, v169
	v_cvt_pk_f16_f32 v169, v170, v171
	ds_write_b64 v164, v[168:169] offset:0
	s_waitcnt vmcnt(10)
	v_cvt_pk_f16_f32 v172, v172, v173
	v_cvt_pk_f16_f32 v173, v174, v175
	ds_write_b64 v164, v[172:173] offset:64
	s_waitcnt vmcnt(9)
	v_cvt_pk_f16_f32 v176, v176, v177
	v_cvt_pk_f16_f32 v177, v178, v179
	ds_write_b64 v164, v[176:177] offset:128
	s_waitcnt vmcnt(8)
	v_cvt_pk_f16_f32 v180, v180, v181
	v_cvt_pk_f16_f32 v181, v182, v183
	ds_write_b64 v164, v[180:181] offset:192
	s_waitcnt lgkmcnt(0)
	s_barrier
	ds_read_b128 v[2:5], v166
	ds_read_b128 v[6:9], v166 offset:32
	ds_read_u16 v10, v167 offset:0
	ds_read_u16 v11, v167 offset:272
	ds_read_u16 v12, v167 offset:544
	ds_read_u16 v13, v167 offset:816
	ds_read_u16 v14, v167 offset:1088
	ds_read_u16 v15, v167 offset:1360
	ds_read_u16 v16, v167 offset:1632
	ds_read_u16 v17, v167 offset:1904
	s_waitcnt lgkmcnt(8)
	global_store_dwordx4 v157, v[2:5], s[36:37] sc1
	global_store_dwordx4 v157, v[6:9], s[36:37] offset:1024 sc1
	s_waitcnt lgkmcnt(0)
	v_lshl_or_b32 v10, v11, 16, v10
	v_lshl_or_b32 v11, v13, 16, v12
	v_lshl_or_b32 v12, v15, 16, v14
	v_lshl_or_b32 v13, v17, 16, v16
	global_store_dwordx4 v157, v[10:13], s[38:39] sc1
	ds_read_u16 v18, v167 offset:4352
	ds_read_u16 v19, v167 offset:4624
	ds_read_u16 v20, v167 offset:4896
	ds_read_u16 v21, v167 offset:5168
	ds_read_u16 v22, v167 offset:5440
	ds_read_u16 v23, v167 offset:5712
	ds_read_u16 v24, v167 offset:5984
	ds_read_u16 v25, v167 offset:6256
	s_waitcnt lgkmcnt(0)
	v_lshl_or_b32 v18, v19, 16, v18
	v_lshl_or_b32 v19, v21, 16, v20
	v_lshl_or_b32 v20, v23, 16, v22
	v_lshl_or_b32 v21, v25, 16, v24
	global_store_dwordx4 v157, v[18:21], s[38:39] offset:1024 sc1
	s_endpgm
